# P7: converted gate/up weight stores marked nt (written once, read two phases later)
# speedup vs baseline: 1.0084x; 1.0031x over previous
; #define LAS __attribute__((address_space(3)))
; DI unsigned pk2(float lo, float hi) { return cvtpk_s(lo, hi); }
; #define LDS_WAIT() asm volatile("s_waitcnt lgkmcnt(0)" ::: "memory")
; template <int MAP>
; DI void cvt_item(const float* W, int N, int ldk, bf16_t* WT, const float* gain, LAS unsigned* scr, int kb, int nb, int lane) {
;     ...
;     for (int j = 0; j < 8; ++j)
; #pragma unroll
;         for (int i = 0; i < 4; ++i) scr[(4 * nq + i) * 32 + ((j ^ (nq & 7)) << 2) + kr] = pk2(v[j][0][i], v[j][1][i]);
;     LDS_WAIT(); asm volatile("" ::: "memory");
; #pragma unroll
;     for (int jj = 0; jj < 8; ++jj) {
;         const int nl = (lane >> 3) + 8 * jj, c = lane & 7;
;         const u32x4 o = *(const LAS u32x4*)(scr + nl * 32 + ((c ^ ((nl >> 2) & 7)) << 2));
;         const int n = n0 + nl;
;         const int row = (MAP == 0) ? n : ((n >> 2) * 8 + (MAP == 2 ? 4 : 0) + (n & 3));
;         *(u32x4*)(WT + (size_t)row * ldk + k0 + 8 * c) = o;
;     }
;     LDS_WAIT(); asm volatile("" ::: "memory");
.LBB0_734:
	s_waitcnt vmcnt(14)
	v_cvt_pk_bf16_f32 v2, v2, v6
	v_add_u32_e32 v6, v137, v138
	v_cvt_pk_bf16_f32 v3, v3, v7
	ds_write2_b32 v6, v2, v3 offset1:32
	v_cvt_pk_bf16_f32 v2, v4, v8
	v_cvt_pk_bf16_f32 v3, v5, v9
	ds_write2_b32 v6, v2, v3 offset0:64 offset1:96
	s_waitcnt vmcnt(12)
	v_cvt_pk_bf16_f32 v2, v10, v14
	v_add_u32_e32 v3, v137, v139
	v_cvt_pk_bf16_f32 v4, v11, v15
	ds_write2_b32 v3, v2, v4 offset1:32
	v_cvt_pk_bf16_f32 v2, v12, v16
	v_cvt_pk_bf16_f32 v4, v13, v17
	ds_write2_b32 v3, v2, v4 offset0:64 offset1:96
	s_waitcnt vmcnt(10)
	v_cvt_pk_bf16_f32 v2, v18, v22
	v_add_u32_e32 v3, v137, v140
	v_cvt_pk_bf16_f32 v4, v19, v23
	ds_write2_b32 v3, v2, v4 offset1:32
	v_cvt_pk_bf16_f32 v2, v20, v24
	v_cvt_pk_bf16_f32 v4, v21, v25
	ds_write2_b32 v3, v2, v4 offset0:64 offset1:96
	s_waitcnt vmcnt(8)
	v_cvt_pk_bf16_f32 v2, v26, v30
	v_add_u32_e32 v3, v137, v141
	v_cvt_pk_bf16_f32 v4, v27, v31
	ds_write2_b32 v3, v2, v4 offset1:32
	v_cvt_pk_bf16_f32 v2, v28, v32
	v_cvt_pk_bf16_f32 v4, v29, v33
	ds_write2_b32 v3, v2, v4 offset0:64 offset1:96
	s_waitcnt vmcnt(6)
	v_cvt_pk_bf16_f32 v2, v34, v38
	v_add_u32_e32 v3, v137, v142
	v_cvt_pk_bf16_f32 v4, v35, v39
	ds_write2_b32 v3, v2, v4 offset1:32
	v_cvt_pk_bf16_f32 v2, v36, v40
	v_cvt_pk_bf16_f32 v4, v37, v41
	ds_write2_b32 v3, v2, v4 offset0:64 offset1:96
	s_waitcnt vmcnt(4)
	v_cvt_pk_bf16_f32 v2, v42, v46
	v_add_u32_e32 v3, v137, v143
	v_cvt_pk_bf16_f32 v4, v43, v47
	ds_write2_b32 v3, v2, v4 offset1:32
	v_cvt_pk_bf16_f32 v2, v44, v48
	v_cvt_pk_bf16_f32 v4, v45, v49
	ds_write2_b32 v3, v2, v4 offset0:64 offset1:96
	s_waitcnt vmcnt(2)
	v_cvt_pk_bf16_f32 v2, v50, v54
	v_add_u32_e32 v3, v137, v144
	v_cvt_pk_bf16_f32 v4, v51, v55
	ds_write2_b32 v3, v2, v4 offset1:32
	v_cvt_pk_bf16_f32 v2, v52, v56
	v_cvt_pk_bf16_f32 v4, v53, v57
	ds_write2_b32 v3, v2, v4 offset0:64 offset1:96
	s_waitcnt vmcnt(0)
	v_cvt_pk_bf16_f32 v2, v58, v62
	v_add_u32_e32 v3, v137, v145
	v_cvt_pk_bf16_f32 v4, v59, v63
	ds_write2_b32 v3, v2, v4 offset1:32
	v_cvt_pk_bf16_f32 v2, v60, v64
	v_cvt_pk_bf16_f32 v4, v61, v65
	ds_write2_b32 v3, v2, v4 offset0:64 offset1:96
	s_waitcnt lgkmcnt(0)
	s_lshl_b32 s10, s36, 1
	ds_read_b128 v[2:5], v148
	v_or_b32_e32 v6, s31, v146
	s_add_u32 s10, s34, s10
	v_lshlrev_b32_e32 v6, 1, v6
	s_addc_u32 s11, s35, 0
	v_lshlrev_b32_e32 v130, 1, v132
	v_and_or_b32 v6, v6, s23, v146
	v_lshl_add_u64 v[10:11], s[10:11], 0, v[130:131]
	v_lshl_or_b32 v130, v6, 12, v163
	v_lshl_add_u64 v[12:13], v[10:11], 0, v[130:131]
	ds_read_b128 v[6:9], v150
	s_waitcnt lgkmcnt(1)
	global_store_dwordx4 v[12:13], v[2:5], off nt
	s_nop 1
	v_or_b32_e32 v2, s31, v149
	v_lshlrev_b32_e32 v2, 1, v2
	v_and_or_b32 v2, v2, s24, v146
	v_lshl_or_b32 v130, v2, 12, v163
	v_lshl_add_u64 v[2:3], v[10:11], 0, v[130:131]
	s_waitcnt lgkmcnt(0)
	global_store_dwordx4 v[2:3], v[6:9], off nt
	ds_read_b128 v[2:5], v152
	s_nop 0
	v_or_b32_e32 v6, s31, v151
	v_lshlrev_b32_e32 v6, 1, v6
	v_and_or_b32 v6, v6, s25, v146
	v_lshl_or_b32 v130, v6, 12, v163
	v_lshl_add_u64 v[12:13], v[10:11], 0, v[130:131]
	ds_read_b128 v[6:9], v154
	s_waitcnt lgkmcnt(1)
	global_store_dwordx4 v[12:13], v[2:5], off nt
	s_nop 1
	v_or_b32_e32 v2, s31, v153
	v_lshlrev_b32_e32 v2, 1, v2
	v_and_or_b32 v2, v2, s26, v146
	v_lshl_or_b32 v130, v2, 12, v163
	v_lshl_add_u64 v[2:3], v[10:11], 0, v[130:131]
	s_waitcnt lgkmcnt(0)
	global_store_dwordx4 v[2:3], v[6:9], off nt
	ds_read_b128 v[2:5], v156
	s_nop 0
	v_or_b32_e32 v6, s31, v155
	v_lshlrev_b32_e32 v6, 1, v6
	v_and_or_b32 v6, v6, s27, v146
	v_lshl_or_b32 v130, v6, 12, v163
	v_lshl_add_u64 v[12:13], v[10:11], 0, v[130:131]
	ds_read_b128 v[6:9], v158
	s_waitcnt lgkmcnt(1)
	global_store_dwordx4 v[12:13], v[2:5], off nt
	s_nop 1
	v_or_b32_e32 v2, s31, v157
	v_lshlrev_b32_e32 v2, 1, v2
	v_and_or_b32 v2, v2, s28, v146
	v_lshl_or_b32 v130, v2, 12, v163
	v_lshl_add_u64 v[2:3], v[10:11], 0, v[130:131]
	s_waitcnt lgkmcnt(0)
	global_store_dwordx4 v[2:3], v[6:9], off nt
	ds_read_b128 v[2:5], v160
	s_nop 0
	v_or_b32_e32 v6, s31, v159
	v_lshlrev_b32_e32 v6, 1, v6
	v_and_or_b32 v6, v6, s29, v146
	v_lshl_or_b32 v130, v6, 12, v163
	v_lshl_add_u64 v[12:13], v[10:11], 0, v[130:131]
	ds_read_b128 v[6:9], v162
	s_waitcnt lgkmcnt(1)
	global_store_dwordx4 v[12:13], v[2:5], off nt
	s_nop 1
	v_or_b32_e32 v2, s31, v161
	v_lshlrev_b32_e32 v2, 1, v2
	v_and_or_b32 v2, v2, s30, v146
	v_lshl_or_b32 v130, v2, 12, v163
	v_lshl_add_u64 v[2:3], v[10:11], 0, v[130:131]
	s_waitcnt lgkmcnt(0)
	global_store_dwordx4 v[2:3], v[6:9], off nt
	s_waitcnt lgkmcnt(0)

; #define LAS __attribute__((address_space(3)))
; DI unsigned pk2(float lo, float hi) { return cvtpk_s(lo, hi); }
; #define LDS_WAIT() asm volatile("s_waitcnt lgkmcnt(0)" ::: "memory")
; template <int MAP>
; DI void cvt_item(const float* W, int N, int ldk, bf16_t* WT, const float* gain, LAS unsigned* scr, int kb, int nb, int lane) {
;     ...
;     for (int j = 0; j < 8; ++j)
; #pragma unroll
;         for (int i = 0; i < 4; ++i) scr[(4 * nq + i) * 32 + ((j ^ (nq & 7)) << 2) + kr] = pk2(v[j][0][i], v[j][1][i]);
;     LDS_WAIT(); asm volatile("" ::: "memory");
; #pragma unroll
;     for (int jj = 0; jj < 8; ++jj) {
;         const int nl = (lane >> 3) + 8 * jj, c = lane & 7;
;         const u32x4 o = *(const LAS u32x4*)(scr + nl * 32 + ((c ^ ((nl >> 2) & 7)) << 2));
;         const int n = n0 + nl;
;         const int row = (MAP == 0) ? n : ((n >> 2) * 8 + (MAP == 2 ? 4 : 0) + (n & 3));
;         *(u32x4*)(WT + (size_t)row * ldk + k0 + 8 * c) = o;
;     }
;     LDS_WAIT(); asm volatile("" ::: "memory");
.LBB0_739:
	v_cvt_pk_bf16_f32 v122, v122, v126
	v_add_u32_e32 v126, v137, v138
	v_cvt_pk_bf16_f32 v123, v123, v127
	v_cvt_pk_bf16_f32 v114, v114, v118
	v_add_u32_e32 v118, v137, v139
	v_cvt_pk_bf16_f32 v115, v115, v119
	v_cvt_pk_bf16_f32 v106, v106, v110
	v_add_u32_e32 v110, v137, v140
	v_cvt_pk_bf16_f32 v107, v107, v111
	v_cvt_pk_bf16_f32 v98, v98, v102
	v_add_u32_e32 v102, v137, v141
	v_cvt_pk_bf16_f32 v99, v99, v103
	v_cvt_pk_bf16_f32 v90, v90, v94
	v_add_u32_e32 v94, v137, v142
	v_cvt_pk_bf16_f32 v91, v91, v95
	v_cvt_pk_bf16_f32 v82, v82, v86
	v_add_u32_e32 v86, v137, v143
	v_cvt_pk_bf16_f32 v83, v83, v87
	v_cvt_pk_bf16_f32 v70, v70, v74
	v_add_u32_e32 v74, v137, v144
	v_cvt_pk_bf16_f32 v71, v71, v75
	ds_write2_b32 v126, v122, v123 offset1:32
	v_cvt_pk_bf16_f32 v122, v124, v128
	v_cvt_pk_bf16_f32 v123, v125, v129
	ds_write2_b32 v118, v114, v115 offset1:32
	v_cvt_pk_bf16_f32 v114, v116, v120
	v_cvt_pk_bf16_f32 v115, v117, v121
	ds_write2_b32 v110, v106, v107 offset1:32
	v_cvt_pk_bf16_f32 v106, v108, v112
	v_cvt_pk_bf16_f32 v107, v109, v113
	ds_write2_b32 v102, v98, v99 offset1:32
	v_cvt_pk_bf16_f32 v98, v100, v104
	v_cvt_pk_bf16_f32 v99, v101, v105
	ds_write2_b32 v94, v90, v91 offset1:32
	v_cvt_pk_bf16_f32 v90, v92, v96
	v_cvt_pk_bf16_f32 v91, v93, v97
	ds_write2_b32 v86, v82, v83 offset1:32
	v_cvt_pk_bf16_f32 v82, v84, v88
	v_cvt_pk_bf16_f32 v83, v85, v89
	ds_write2_b32 v74, v70, v71 offset1:32
	v_cvt_pk_bf16_f32 v70, v72, v76
	v_cvt_pk_bf16_f32 v71, v73, v77
	ds_write2_b32 v126, v122, v123 offset0:64 offset1:96
	ds_write2_b32 v118, v114, v115 offset0:64 offset1:96
	ds_write2_b32 v110, v106, v107 offset0:64 offset1:96
	ds_write2_b32 v102, v98, v99 offset0:64 offset1:96
	ds_write2_b32 v94, v90, v91 offset0:64 offset1:96
	ds_write2_b32 v86, v82, v83 offset0:64 offset1:96
	ds_write2_b32 v74, v70, v71 offset0:64 offset1:96
	v_cvt_pk_bf16_f32 v66, v66, v78
	v_add_u32_e32 v70, v137, v145
	v_cvt_pk_bf16_f32 v67, v67, v79
	ds_write2_b32 v70, v66, v67 offset1:32
	v_cvt_pk_bf16_f32 v66, v68, v80
	v_cvt_pk_bf16_f32 v67, v69, v81
	ds_write2_b32 v70, v66, v67 offset0:64 offset1:96
	s_waitcnt lgkmcnt(0)
	s_lshl_b32 s10, s36, 1
	ds_read_b128 v[66:69], v148
	v_or_b32_e32 v70, s31, v146
	s_add_u32 s10, s34, s10
	v_lshlrev_b32_e32 v70, 1, v70
	s_addc_u32 s11, s35, 0
	v_lshlrev_b32_e32 v130, 1, v132
	v_and_or_b32 v70, v70, s23, v147
	v_lshl_add_u64 v[74:75], s[10:11], 0, v[130:131]
	v_lshlrev_b32_e32 v130, 12, v70
	v_lshl_add_u64 v[76:77], v[74:75], 0, v[130:131]
	ds_read_b128 v[70:73], v150
	s_waitcnt lgkmcnt(1)
	global_store_dwordx4 v[76:77], v[66:69], off nt
	s_nop 1
	v_or_b32_e32 v66, s31, v149
	v_lshlrev_b32_e32 v66, 1, v66
	v_and_or_b32 v66, v66, s24, v147
	v_lshlrev_b32_e32 v130, 12, v66
	v_lshl_add_u64 v[66:67], v[74:75], 0, v[130:131]
	s_waitcnt lgkmcnt(0)
	global_store_dwordx4 v[66:67], v[70:73], off nt
	ds_read_b128 v[66:69], v152
	s_nop 0
	v_or_b32_e32 v70, s31, v151
	v_lshlrev_b32_e32 v70, 1, v70
	v_and_or_b32 v70, v70, s25, v147
	v_lshlrev_b32_e32 v130, 12, v70
	v_lshl_add_u64 v[76:77], v[74:75], 0, v[130:131]
	ds_read_b128 v[70:73], v154
	s_waitcnt lgkmcnt(1)
	global_store_dwordx4 v[76:77], v[66:69], off nt
	s_nop 1
	v_or_b32_e32 v66, s31, v153
	v_lshlrev_b32_e32 v66, 1, v66
	v_and_or_b32 v66, v66, s26, v147
	v_lshlrev_b32_e32 v130, 12, v66
	v_lshl_add_u64 v[66:67], v[74:75], 0, v[130:131]
	s_waitcnt lgkmcnt(0)
	global_store_dwordx4 v[66:67], v[70:73], off nt
	ds_read_b128 v[66:69], v156
	s_nop 0
	v_or_b32_e32 v70, s31, v155
	v_lshlrev_b32_e32 v70, 1, v70
	v_and_or_b32 v70, v70, s27, v147
	v_lshlrev_b32_e32 v130, 12, v70
	v_lshl_add_u64 v[76:77], v[74:75], 0, v[130:131]
	ds_read_b128 v[70:73], v158
	s_waitcnt lgkmcnt(1)
	global_store_dwordx4 v[76:77], v[66:69], off nt
	s_nop 1
	v_or_b32_e32 v66, s31, v157
	v_lshlrev_b32_e32 v66, 1, v66
	v_and_or_b32 v66, v66, s28, v147
	v_lshlrev_b32_e32 v130, 12, v66
	v_lshl_add_u64 v[66:67], v[74:75], 0, v[130:131]
	s_waitcnt lgkmcnt(0)
	global_store_dwordx4 v[66:67], v[70:73], off nt
	ds_read_b128 v[66:69], v160
	s_nop 0
	v_or_b32_e32 v70, s31, v159
	v_lshlrev_b32_e32 v70, 1, v70
	v_and_or_b32 v70, v70, s29, v147
	v_lshlrev_b32_e32 v130, 12, v70
	v_lshl_add_u64 v[76:77], v[74:75], 0, v[130:131]
	ds_read_b128 v[70:73], v162
	s_waitcnt lgkmcnt(1)
	global_store_dwordx4 v[76:77], v[66:69], off nt
	s_nop 1
	v_or_b32_e32 v66, s31, v161
	v_lshlrev_b32_e32 v66, 1, v66
	v_and_or_b32 v66, v66, s30, v147
	v_lshlrev_b32_e32 v130, 12, v66
	v_lshl_add_u64 v[66:67], v[74:75], 0, v[130:131]
	s_waitcnt lgkmcnt(0)
	global_store_dwordx4 v[66:67], v[70:73], off nt
	s_waitcnt lgkmcnt(0)
	s_branch .LBB0_735
